# P2 K-loop: loader wave raised to s_setprio 2 during its load segment (MFMA partner stays at 1)
# baseline (speedup 1.0000x reference)
.LBB0_238:
	s_setprio 2
	ds_read_b128 v[20:23], v203
	ds_read_b128 v[34:37], v203 offset:1024
	ds_read_b128 v[38:41], v203 offset:2048
	ds_read_b128 v[208:211], v203 offset:3072
	ds_read_b128 v[212:215], v207
	ds_read_b128 v[216:219], v207 offset:1024
	ds_read_b128 v[226:229], v207 offset:2048
	ds_read_b128 v[230:233], v207 offset:3072
	s_add_u32 s28, s10, 0xfffc0080
	s_addc_u32 s29, s11, -1
	s_cmp_eq_u32 s39, 12
	s_cselect_b32 s49, s2, s29
	s_cselect_b32 s48, s3, s28
	s_cselect_b32 s47, s13, s33
	s_cselect_b32 s46, s15, s20
	v_lshl_add_u64 v[24:25], s[10:11], 0, v[174:175]
	s_add_i32 m0, s58, 0xc000
	ds_read_b128 v[234:237], v224
	ds_read_b128 v[238:241], v224 offset:1024
	ds_read_b128 v[242:245], v224 offset:2048
	ds_read_b128 v[246:249], v224 offset:3072
	ds_read_b128 v[250:253], v224 offset:4096
	ds_read_b128 v[220:223], v224 offset:5120
	ds_read_b128 v[178:181], v224 offset:6144
	ds_read_b128 v[196:199], v224 offset:7168
	global_load_lds_dwordx4 v[24:25], off
	v_lshl_add_u64 v[24:25], s[10:11], 0, v[176:177]
	s_add_i32 m0, s58, 0xe000
	s_nop 0
	global_load_lds_dwordx4 v[24:25], off
	s_waitcnt vmcnt(8)
	s_waitcnt lgkmcnt(0)
	s_barrier
	s_setprio 1
	s_waitcnt lgkmcnt(0)
	v_mfma_i32_16x16x64_i8 v[142:145], v[20:23], v[234:237], v[142:145]
	v_mfma_i32_16x16x64_i8 v[138:141], v[38:41], v[234:237], v[138:141]
	v_mfma_i32_16x16x64_i8 v[126:129], v[20:23], v[242:245], v[126:129]
	v_mfma_i32_16x16x64_i8 v[122:125], v[38:41], v[242:245], v[122:125]
	v_mfma_i32_16x16x64_i8 v[110:113], v[20:23], v[250:253], v[110:113]
	v_mfma_i32_16x16x64_i8 v[106:109], v[38:41], v[250:253], v[106:109]
	v_mfma_i32_16x16x64_i8 v[94:97], v[20:23], v[178:181], v[94:97]
	v_mfma_i32_16x16x64_i8 v[90:93], v[38:41], v[178:181], v[90:93]
	v_mfma_i32_16x16x64_i8 v[142:145], v[34:37], v[238:241], v[142:145]
	v_mfma_i32_16x16x64_i8 v[138:141], v[208:211], v[238:241], v[138:141]
	v_mfma_i32_16x16x64_i8 v[126:129], v[34:37], v[246:249], v[126:129]
	v_mfma_i32_16x16x64_i8 v[122:125], v[208:211], v[246:249], v[122:125]
	v_mfma_i32_16x16x64_i8 v[110:113], v[34:37], v[220:223], v[110:113]
	v_mfma_i32_16x16x64_i8 v[106:109], v[208:211], v[220:223], v[106:109]
	v_mfma_i32_16x16x64_i8 v[94:97], v[34:37], v[196:199], v[94:97]
	v_mfma_i32_16x16x64_i8 v[90:93], v[208:211], v[196:199], v[90:93]
	s_setprio 0
	s_setprio 1
	v_mfma_i32_16x16x64_i8 v[134:137], v[212:215], v[234:237], v[134:137]
	v_mfma_i32_16x16x64_i8 v[130:133], v[226:229], v[234:237], v[130:133]
	v_mfma_i32_16x16x64_i8 v[118:121], v[212:215], v[242:245], v[118:121]
	v_mfma_i32_16x16x64_i8 v[114:117], v[226:229], v[242:245], v[114:117]
	v_mfma_i32_16x16x64_i8 v[102:105], v[212:215], v[250:253], v[102:105]
	v_mfma_i32_16x16x64_i8 v[98:101], v[226:229], v[250:253], v[98:101]
	v_mfma_i32_16x16x64_i8 v[86:89], v[212:215], v[178:181], v[86:89]
	v_mfma_i32_16x16x64_i8 v[82:85], v[226:229], v[178:181], v[82:85]
	v_mfma_i32_16x16x64_i8 v[134:137], v[216:219], v[238:241], v[134:137]
	v_mfma_i32_16x16x64_i8 v[130:133], v[230:233], v[238:241], v[130:133]
	v_mfma_i32_16x16x64_i8 v[118:121], v[216:219], v[246:249], v[118:121]
	v_mfma_i32_16x16x64_i8 v[114:117], v[230:233], v[246:249], v[114:117]
	v_mfma_i32_16x16x64_i8 v[102:105], v[216:219], v[220:223], v[102:105]
	v_mfma_i32_16x16x64_i8 v[98:101], v[230:233], v[220:223], v[98:101]
	v_mfma_i32_16x16x64_i8 v[86:89], v[216:219], v[196:199], v[86:89]
	v_mfma_i32_16x16x64_i8 v[82:85], v[230:233], v[196:199], v[82:85]
	s_setprio 0
	s_barrier
	s_setprio 2
	s_add_i32 s28, s80, s57
	v_lshl_add_u64 v[184:185], s[46:47], 0, v[148:149]
	s_mov_b32 m0, s28
	ds_read_b128 v[178:181], v224 offset:16384
	ds_read_b128 v[196:199], v224 offset:17408
	ds_read_b128 v[220:223], v224 offset:18432
	ds_read_b128 v[234:237], v224 offset:19456
	ds_read_b128 v[238:241], v224 offset:20480
	ds_read_b128 v[242:245], v224 offset:21504
	ds_read_b128 v[246:249], v224 offset:22528
	ds_read_b128 v[250:253], v224 offset:23552
	global_load_lds_dwordx4 v[184:185], off
	s_add_i32 m0, s28, 0x2000
	s_add_u32 s28, s46, 0x40000
	v_lshl_add_u64 v[188:189], s[46:47], 0, v[152:153]
	s_addc_u32 s29, s47, 0
	s_add_i32 s41, s81, s57
	global_load_lds_dwordx4 v[188:189], off
	v_lshl_add_u64 v[24:25], s[28:29], 0, v[148:149]
	s_mov_b32 m0, s41
	v_lshl_add_u64 v[192:193], s[48:49], 0, v[146:147]
	global_load_lds_dwordx4 v[24:25], off
	v_lshl_add_u64 v[24:25], s[28:29], 0, v[152:153]
	s_add_i32 m0, s41, 0x2000
	v_lshl_add_u64 v[200:201], s[48:49], 0, v[150:151]
	global_load_lds_dwordx4 v[24:25], off
	s_mov_b32 m0, s58
	s_nop 0
	global_load_lds_dwordx4 v[192:193], off
	s_mov_b32 m0, s59
	s_nop 0
	global_load_lds_dwordx4 v[200:201], off
	s_waitcnt vmcnt(8)
	s_waitcnt lgkmcnt(0)
	s_barrier
	s_setprio 1
	s_waitcnt lgkmcnt(0)
	v_mfma_i32_16x16x64_i8 v[78:81], v[20:23], v[178:181], v[78:81]
	v_mfma_i32_16x16x64_i8 v[74:77], v[38:41], v[178:181], v[74:77]
	v_mfma_i32_16x16x64_i8 v[62:65], v[20:23], v[220:223], v[62:65]
	v_mfma_i32_16x16x64_i8 v[58:61], v[38:41], v[220:223], v[58:61]
	v_mfma_i32_16x16x64_i8 v[46:49], v[20:23], v[238:241], v[46:49]
	v_mfma_i32_16x16x64_i8 v[42:45], v[38:41], v[238:241], v[42:45]
	v_mfma_i32_16x16x64_i8 v[14:17], v[20:23], v[246:249], v[14:17]
	v_mfma_i32_16x16x64_i8 v[10:13], v[38:41], v[246:249], v[10:13]
	v_mfma_i32_16x16x64_i8 v[78:81], v[34:37], v[196:199], v[78:81]
	v_mfma_i32_16x16x64_i8 v[74:77], v[208:211], v[196:199], v[74:77]
	v_mfma_i32_16x16x64_i8 v[62:65], v[34:37], v[234:237], v[62:65]
	v_mfma_i32_16x16x64_i8 v[58:61], v[208:211], v[234:237], v[58:61]
	v_mfma_i32_16x16x64_i8 v[46:49], v[34:37], v[242:245], v[46:49]
	v_mfma_i32_16x16x64_i8 v[42:45], v[208:211], v[242:245], v[42:45]
	v_mfma_i32_16x16x64_i8 v[14:17], v[34:37], v[250:253], v[14:17]
	v_mfma_i32_16x16x64_i8 v[10:13], v[208:211], v[250:253], v[10:13]
	s_setprio 0
	s_setprio 1
	v_mfma_i32_16x16x64_i8 v[50:53], v[226:229], v[220:223], v[50:53]
	v_mfma_i32_16x16x64_i8 v[30:33], v[212:215], v[238:241], v[30:33]
	v_mfma_i32_16x16x64_i8 v[24:27], v[226:229], v[238:241], v[26:29]
	v_mfma_i32_16x16x64_i8 v[6:9], v[212:215], v[246:249], v[6:9]
	v_mfma_i32_16x16x64_i8 v[2:5], v[226:229], v[246:249], v[2:5]
	v_mfma_i32_16x16x64_i8 v[20:23], v[212:215], v[178:181], v[70:73]
	v_mfma_i32_16x16x64_i8 v[34:37], v[226:229], v[178:181], v[66:69]
	v_mfma_i32_16x16x64_i8 v[38:41], v[212:215], v[220:223], v[54:57]
	v_mfma_i32_16x16x64_i8 v[50:53], v[230:233], v[234:237], v[50:53]
	v_mfma_i32_16x16x64_i8 v[30:33], v[216:219], v[242:245], v[30:33]
	v_mfma_i32_16x16x64_i8 v[24:27], v[230:233], v[242:245], v[24:27]
	v_mfma_i32_16x16x64_i8 v[6:9], v[216:219], v[250:253], v[6:9]
	v_mfma_i32_16x16x64_i8 v[2:5], v[230:233], v[250:253], v[2:5]
	v_mfma_i32_16x16x64_i8 v[20:23], v[216:219], v[196:199], v[20:23]
	v_mfma_i32_16x16x64_i8 v[34:37], v[230:233], v[196:199], v[34:37]
	v_mfma_i32_16x16x64_i8 v[38:41], v[216:219], v[234:237], v[38:41]
	s_setprio 0
	s_barrier
	s_setprio 2
	s_add_i32 s41, 0, 0x18000
	v_add_u32_e32 v28, s41, v183
	s_add_i32 s50, 0, 0x1c000
	ds_read_b128 v[54:57], v28
	ds_read_b128 v[66:69], v28 offset:1024
	ds_read_b128 v[70:73], v28 offset:2048
	ds_read_b128 v[178:181], v28 offset:3072
	v_add_u32_e32 v28, s50, v183
	ds_read_b128 v[196:199], v28
	ds_read_b128 v[208:211], v28 offset:1024
	ds_read_b128 v[212:215], v28 offset:2048
	ds_read_b128 v[216:219], v28 offset:3072
	s_add_u32 s28, s48, 0x40000
	s_addc_u32 s29, s49, 0
	s_mov_b32 m0, s60
	v_lshl_add_u64 v[28:29], s[28:29], 0, v[146:147]
	ds_read_b128 v[220:223], v224 offset:32768
	ds_read_b128 v[226:229], v224 offset:33792
	ds_read_b128 v[230:233], v224 offset:34816
	ds_read_b128 v[234:237], v224 offset:35840
	ds_read_b128 v[238:241], v224 offset:36864
	ds_read_b128 v[242:245], v224 offset:37888
	ds_read_b128 v[246:249], v224 offset:38912
	ds_read_b128 v[250:253], v224 offset:39936
	global_load_lds_dwordx4 v[28:29], off
	v_lshl_add_u64 v[28:29], s[28:29], 0, v[150:151]
	s_mov_b32 m0, s61
	s_nop 0
	global_load_lds_dwordx4 v[28:29], off
	s_waitcnt vmcnt(8)
	s_waitcnt lgkmcnt(0)
	s_barrier
	s_setprio 1
	s_waitcnt lgkmcnt(0)
	v_mfma_i32_16x16x64_i8 v[142:145], v[54:57], v[220:223], v[142:145]
	v_mfma_i32_16x16x64_i8 v[138:141], v[70:73], v[220:223], v[138:141]
	v_mfma_i32_16x16x64_i8 v[126:129], v[54:57], v[230:233], v[126:129]
	v_mfma_i32_16x16x64_i8 v[122:125], v[70:73], v[230:233], v[122:125]
	v_mfma_i32_16x16x64_i8 v[110:113], v[54:57], v[238:241], v[110:113]
	v_mfma_i32_16x16x64_i8 v[106:109], v[70:73], v[238:241], v[106:109]
	v_mfma_i32_16x16x64_i8 v[94:97], v[54:57], v[246:249], v[94:97]
	v_mfma_i32_16x16x64_i8 v[90:93], v[70:73], v[246:249], v[90:93]
	v_mfma_i32_16x16x64_i8 v[142:145], v[66:69], v[226:229], v[142:145]
	v_mfma_i32_16x16x64_i8 v[138:141], v[178:181], v[226:229], v[138:141]
	v_mfma_i32_16x16x64_i8 v[126:129], v[66:69], v[234:237], v[126:129]
	v_mfma_i32_16x16x64_i8 v[122:125], v[178:181], v[234:237], v[122:125]
	v_mfma_i32_16x16x64_i8 v[110:113], v[66:69], v[242:245], v[110:113]
	v_mfma_i32_16x16x64_i8 v[106:109], v[178:181], v[242:245], v[106:109]
	v_mfma_i32_16x16x64_i8 v[94:97], v[66:69], v[250:253], v[94:97]
	v_mfma_i32_16x16x64_i8 v[90:93], v[178:181], v[250:253], v[90:93]
	s_setprio 0
	s_setprio 1
	v_mfma_i32_16x16x64_i8 v[134:137], v[196:199], v[220:223], v[134:137]
	v_mfma_i32_16x16x64_i8 v[130:133], v[212:215], v[220:223], v[130:133]
	v_mfma_i32_16x16x64_i8 v[118:121], v[196:199], v[230:233], v[118:121]
	v_mfma_i32_16x16x64_i8 v[114:117], v[212:215], v[230:233], v[114:117]
	v_mfma_i32_16x16x64_i8 v[102:105], v[196:199], v[238:241], v[102:105]
	v_mfma_i32_16x16x64_i8 v[98:101], v[212:215], v[238:241], v[98:101]
	v_mfma_i32_16x16x64_i8 v[86:89], v[196:199], v[246:249], v[86:89]
	v_mfma_i32_16x16x64_i8 v[82:85], v[212:215], v[246:249], v[82:85]
	v_mfma_i32_16x16x64_i8 v[134:137], v[208:211], v[226:229], v[134:137]
	v_mfma_i32_16x16x64_i8 v[130:133], v[216:219], v[226:229], v[130:133]
	v_mfma_i32_16x16x64_i8 v[118:121], v[208:211], v[234:237], v[118:121]
	v_mfma_i32_16x16x64_i8 v[114:117], v[216:219], v[234:237], v[114:117]
	v_mfma_i32_16x16x64_i8 v[102:105], v[208:211], v[242:245], v[102:105]
	v_mfma_i32_16x16x64_i8 v[98:101], v[216:219], v[242:245], v[98:101]
	v_mfma_i32_16x16x64_i8 v[86:89], v[208:211], v[250:253], v[86:89]
	v_mfma_i32_16x16x64_i8 v[82:85], v[216:219], v[250:253], v[82:85]
	s_setprio 0
	s_barrier
	s_setprio 2
	s_add_i32 s28, s41, s57
	v_lshl_add_u64 v[28:29], v[184:185], 0, s[24:25]
	s_mov_b32 m0, s28
	ds_read_b128 v[220:223], v224 offset:49152
	ds_read_b128 v[226:229], v224 offset:50176
	ds_read_b128 v[230:233], v224 offset:51200
	ds_read_b128 v[234:237], v224 offset:52224
	ds_read_b128 v[238:241], v224 offset:53248
	ds_read_b128 v[242:245], v224 offset:54272
	ds_read_b128 v[246:249], v224 offset:55296
	ds_read_b128 v[250:253], v224 offset:56320
	global_load_lds_dwordx4 v[28:29], off
	s_add_i32 m0, s28, 0x2000
	s_add_u32 s28, s46, 0x40080
	v_lshl_add_u64 v[28:29], v[188:189], 0, s[24:25]
	s_addc_u32 s29, s47, 0
	s_add_i32 s41, s50, s57
	global_load_lds_dwordx4 v[28:29], off
	v_lshl_add_u64 v[28:29], s[28:29], 0, v[148:149]
	s_mov_b32 m0, s41
	s_nop 0
	global_load_lds_dwordx4 v[28:29], off
	v_lshl_add_u64 v[28:29], s[28:29], 0, v[152:153]
	s_add_i32 m0, s41, 0x2000
	s_nop 0
	global_load_lds_dwordx4 v[28:29], off
	v_lshl_add_u64 v[28:29], v[192:193], 0, s[24:25]
	s_mov_b32 m0, s64
	s_nop 0
	global_load_lds_dwordx4 v[28:29], off
	v_lshl_add_u64 v[28:29], v[200:201], 0, s[24:25]
	s_mov_b32 m0, s65
	s_nop 0
	global_load_lds_dwordx4 v[28:29], off
	s_waitcnt vmcnt(8)
	s_waitcnt lgkmcnt(0)
	s_barrier
	s_setprio 1
	s_waitcnt lgkmcnt(0)
	v_mfma_i32_16x16x64_i8 v[78:81], v[54:57], v[220:223], v[78:81]
	v_mfma_i32_16x16x64_i8 v[74:77], v[70:73], v[220:223], v[74:77]
	v_mfma_i32_16x16x64_i8 v[62:65], v[54:57], v[230:233], v[62:65]
	v_mfma_i32_16x16x64_i8 v[58:61], v[70:73], v[230:233], v[58:61]
	v_mfma_i32_16x16x64_i8 v[46:49], v[54:57], v[238:241], v[46:49]
	v_mfma_i32_16x16x64_i8 v[42:45], v[70:73], v[238:241], v[42:45]
	v_mfma_i32_16x16x64_i8 v[14:17], v[54:57], v[246:249], v[14:17]
	v_mfma_i32_16x16x64_i8 v[10:13], v[70:73], v[246:249], v[10:13]
	v_mfma_i32_16x16x64_i8 v[78:81], v[66:69], v[226:229], v[78:81]
	v_mfma_i32_16x16x64_i8 v[74:77], v[178:181], v[226:229], v[74:77]
	v_mfma_i32_16x16x64_i8 v[62:65], v[66:69], v[234:237], v[62:65]
	v_mfma_i32_16x16x64_i8 v[58:61], v[178:181], v[234:237], v[58:61]
	v_mfma_i32_16x16x64_i8 v[46:49], v[66:69], v[242:245], v[46:49]
	v_mfma_i32_16x16x64_i8 v[42:45], v[178:181], v[242:245], v[42:45]
	v_mfma_i32_16x16x64_i8 v[14:17], v[66:69], v[250:253], v[14:17]
	v_mfma_i32_16x16x64_i8 v[10:13], v[178:181], v[250:253], v[10:13]
	s_setprio 0
	s_setprio 1
	v_mfma_i32_16x16x64_i8 v[20:23], v[196:199], v[220:223], v[20:23]
	v_mfma_i32_16x16x64_i8 v[70:73], v[208:211], v[226:229], v[20:23]
	v_mfma_i32_16x16x64_i8 v[20:23], v[212:215], v[220:223], v[34:37]
	v_mfma_i32_16x16x64_i8 v[66:69], v[216:219], v[226:229], v[20:23]
	v_mfma_i32_16x16x64_i8 v[20:23], v[196:199], v[230:233], v[38:41]
	v_mfma_i32_16x16x64_i8 v[54:57], v[208:211], v[234:237], v[20:23]
	v_mfma_i32_16x16x64_i8 v[20:23], v[212:215], v[230:233], v[50:53]
	v_mfma_i32_16x16x64_i8 v[50:53], v[216:219], v[234:237], v[20:23]
	v_mfma_i32_16x16x64_i8 v[20:23], v[196:199], v[238:241], v[30:33]
	v_mfma_i32_16x16x64_i8 v[30:33], v[208:211], v[242:245], v[20:23]
	v_mfma_i32_16x16x64_i8 v[20:23], v[212:215], v[238:241], v[24:27]
	v_mfma_i32_16x16x64_i8 v[6:9], v[196:199], v[246:249], v[6:9]
	v_mfma_i32_16x16x64_i8 v[2:5], v[212:215], v[246:249], v[2:5]
	v_mfma_i32_16x16x64_i8 v[26:29], v[216:219], v[242:245], v[20:23]
	v_mfma_i32_16x16x64_i8 v[6:9], v[208:211], v[250:253], v[6:9]
	v_mfma_i32_16x16x64_i8 v[2:5], v[216:219], v[250:253], v[2:5]
	s_setprio 0
	s_barrier
	s_add_i32 s39, s39, 2
	s_add_u32 s10, s10, 0x100
	s_addc_u32 s11, s11, 0
	s_add_u32 s20, s20, 0x100
	s_addc_u32 s33, s33, 0
	s_cmp_gt_u32 s39, 13
	s_cbranch_scc0 .LBB0_238
	s_and_b64 vcc, exec, s[26:27]
	s_cbranch_vccz .LBB0_241
	s_barrier
